# P3 deferred w_up/w_down conversion items: next round's source tile touched into L2 (two dword loads per lane) right after this item's loads; counted waits +2; on top of v11
# baseline (speedup 1.0000x reference)
; #define GAS __attribute__((address_space(1)))
; #define LAS __attribute__((address_space(3)))
;     const int nblk = N / 64, kb = item / nblk, nb = item - kb * nblk, k0 = 64 * kb, n0 = 64 * nb; if (ldw == 0) ldw = N;
;     const int c4 = lane & 15, kq = lane >> 4;
; #pragma unroll 4
;     for (int i = 0; i < 16; ++i) { const int kk = 4 * i + kq;
;         f32x4 v = __builtin_nontemporal_load((const GAS f32x4*)(W + (size_t)(k0 + kk) * ldw + n0 + 4 * c4));
;         v = v * (gk ? gk[k0 + kk] * scale : scale);
;         LAS float* d = scr + kk * 65 + 4 * c4; d[0] = v[0]; d[1] = v[1]; d[2] = v[2]; d[3] = v[3]; }
.LBB0_986:
	s_mov_b32 s100, 0x10000
	s_mov_b32 s101, 0
	global_load_dwordx4 v[64:67], v[12:13], off nt
	v_lshl_add_u64 v[12:13], v[12:13], 0, s[100:101]
	global_load_dwordx4 v[68:71], v[12:13], off nt
	v_lshl_add_u64 v[12:13], v[12:13], 0, s[100:101]
	global_load_dwordx4 v[72:75], v[12:13], off nt
	v_lshl_add_u64 v[12:13], v[12:13], 0, s[100:101]
	global_load_dwordx4 v[76:79], v[12:13], off nt
	v_lshl_add_u64 v[12:13], v[12:13], 0, s[100:101]
	global_load_dwordx4 v[80:83], v[12:13], off nt
	v_lshl_add_u64 v[12:13], v[12:13], 0, s[100:101]
	global_load_dwordx4 v[84:87], v[12:13], off nt
	v_lshl_add_u64 v[12:13], v[12:13], 0, s[100:101]
	global_load_dwordx4 v[88:91], v[12:13], off nt
	v_lshl_add_u64 v[12:13], v[12:13], 0, s[100:101]
	global_load_dwordx4 v[92:95], v[12:13], off nt
	v_lshl_add_u64 v[12:13], v[12:13], 0, s[100:101]
	global_load_dwordx4 v[96:99], v[12:13], off nt
	v_lshl_add_u64 v[12:13], v[12:13], 0, s[100:101]
	global_load_dwordx4 v[100:103], v[12:13], off nt
	v_lshl_add_u64 v[12:13], v[12:13], 0, s[100:101]
	global_load_dwordx4 v[104:107], v[12:13], off nt
	v_lshl_add_u64 v[12:13], v[12:13], 0, s[100:101]
	global_load_dwordx4 v[108:111], v[12:13], off nt
	v_lshl_add_u64 v[12:13], v[12:13], 0, s[100:101]
	global_load_dwordx4 v[112:115], v[12:13], off nt
	v_lshl_add_u64 v[12:13], v[12:13], 0, s[100:101]
	global_load_dwordx4 v[116:119], v[12:13], off nt
	v_lshl_add_u64 v[12:13], v[12:13], 0, s[100:101]
	global_load_dwordx4 v[120:123], v[12:13], off nt
	v_lshl_add_u64 v[12:13], v[12:13], 0, s[100:101]
	global_load_dwordx4 v[124:127], v[12:13], off nt
	s_cmp_lt_u32 s29, 0x9000
	s_cselect_b64 s[98:99], -1, 0
	v_lshrrev_b32_e32 v195, 4, v23
	v_sub_u32_e32 v196, v23, v195
	v_lshlrev_b32_e32 v196, 14, v196
	v_and_b32_e32 v195, 15, v23
	v_lshlrev_b32_e32 v195, 4, v195
	v_sub_u32_e32 v196, v196, v195
	v_add_u32_e32 v196, 0x1f10000, v196
	v_mov_b32_e32 v195, 0xffffff80
	v_cndmask_b32_e64 v196, v195, v196, s[98:99]
	v_ashrrev_i32_e32 v197, 31, v196
	v_lshl_add_u64 v[196:197], v[12:13], 0, v[196:197]
	global_load_dword v195, v[196:197], off
	global_load_dword v195, v[196:197], off offset:128
	s_waitcnt vmcnt(17)
	v_pk_mul_f32 v[64:65], v[64:65], s[94:95] op_sel_hi:[1,0]
	v_pk_mul_f32 v[66:67], v[66:67], s[94:95] op_sel_hi:[1,0]
	ds_write2_b32 v15, v64, v65 offset1:1
	ds_write2_b32 v15, v66, v67 offset0:2 offset1:3
	s_waitcnt vmcnt(16)
	v_pk_mul_f32 v[68:69], v[68:69], s[94:95] op_sel_hi:[1,0]
	v_pk_mul_f32 v[70:71], v[70:71], s[94:95] op_sel_hi:[1,0]
	v_add_u32_e32 v2, 0x410, v15
	ds_write2_b32 v2, v68, v69 offset1:1
	ds_write2_b32 v2, v70, v71 offset0:2 offset1:3
	s_waitcnt vmcnt(15)
	v_pk_mul_f32 v[72:73], v[72:73], s[94:95] op_sel_hi:[1,0]
	v_pk_mul_f32 v[74:75], v[74:75], s[94:95] op_sel_hi:[1,0]
	v_add_u32_e32 v2, 0x820, v15
	ds_write2_b32 v2, v72, v73 offset1:1
	ds_write2_b32 v2, v74, v75 offset0:2 offset1:3
	s_waitcnt vmcnt(14)
	v_pk_mul_f32 v[76:77], v[76:77], s[94:95] op_sel_hi:[1,0]
	v_pk_mul_f32 v[78:79], v[78:79], s[94:95] op_sel_hi:[1,0]
	v_add_u32_e32 v2, 0xc30, v15
	ds_write2_b32 v2, v76, v77 offset1:1
	ds_write2_b32 v2, v78, v79 offset0:2 offset1:3
	s_waitcnt vmcnt(13)
	v_pk_mul_f32 v[80:81], v[80:81], s[94:95] op_sel_hi:[1,0]
	v_pk_mul_f32 v[82:83], v[82:83], s[94:95] op_sel_hi:[1,0]
	v_add_u32_e32 v2, 0x1040, v15
	ds_write2_b32 v2, v80, v81 offset1:1
	ds_write2_b32 v2, v82, v83 offset0:2 offset1:3
	s_waitcnt vmcnt(12)
	v_pk_mul_f32 v[84:85], v[84:85], s[94:95] op_sel_hi:[1,0]
	v_pk_mul_f32 v[86:87], v[86:87], s[94:95] op_sel_hi:[1,0]
	v_add_u32_e32 v2, 0x1450, v15
	ds_write2_b32 v2, v84, v85 offset1:1
	ds_write2_b32 v2, v86, v87 offset0:2 offset1:3
	s_waitcnt vmcnt(11)
	v_pk_mul_f32 v[88:89], v[88:89], s[94:95] op_sel_hi:[1,0]
	v_pk_mul_f32 v[90:91], v[90:91], s[94:95] op_sel_hi:[1,0]
	v_add_u32_e32 v2, 0x1860, v15
	ds_write2_b32 v2, v88, v89 offset1:1
	ds_write2_b32 v2, v90, v91 offset0:2 offset1:3
	s_waitcnt vmcnt(10)
	v_pk_mul_f32 v[92:93], v[92:93], s[94:95] op_sel_hi:[1,0]
	v_pk_mul_f32 v[94:95], v[94:95], s[94:95] op_sel_hi:[1,0]
	v_add_u32_e32 v2, 0x1c70, v15
	ds_write2_b32 v2, v92, v93 offset1:1
	ds_write2_b32 v2, v94, v95 offset0:2 offset1:3
	s_waitcnt vmcnt(9)
	v_pk_mul_f32 v[96:97], v[96:97], s[94:95] op_sel_hi:[1,0]
	v_pk_mul_f32 v[98:99], v[98:99], s[94:95] op_sel_hi:[1,0]
	v_add_u32_e32 v2, 0x2080, v15
	ds_write2_b32 v2, v96, v97 offset1:1
	ds_write2_b32 v2, v98, v99 offset0:2 offset1:3
	s_waitcnt vmcnt(8)
	v_pk_mul_f32 v[100:101], v[100:101], s[94:95] op_sel_hi:[1,0]
	v_pk_mul_f32 v[102:103], v[102:103], s[94:95] op_sel_hi:[1,0]
	v_add_u32_e32 v2, 0x2490, v15
	ds_write2_b32 v2, v100, v101 offset1:1
	ds_write2_b32 v2, v102, v103 offset0:2 offset1:3
	s_waitcnt vmcnt(7)
	v_pk_mul_f32 v[104:105], v[104:105], s[94:95] op_sel_hi:[1,0]
	v_pk_mul_f32 v[106:107], v[106:107], s[94:95] op_sel_hi:[1,0]
	v_add_u32_e32 v2, 0x28a0, v15
	ds_write2_b32 v2, v104, v105 offset1:1
	ds_write2_b32 v2, v106, v107 offset0:2 offset1:3
	s_waitcnt vmcnt(6)
	v_pk_mul_f32 v[108:109], v[108:109], s[94:95] op_sel_hi:[1,0]
	v_pk_mul_f32 v[110:111], v[110:111], s[94:95] op_sel_hi:[1,0]
	v_add_u32_e32 v2, 0x2cb0, v15
	ds_write2_b32 v2, v108, v109 offset1:1
	ds_write2_b32 v2, v110, v111 offset0:2 offset1:3
	s_waitcnt vmcnt(5)
	v_pk_mul_f32 v[112:113], v[112:113], s[94:95] op_sel_hi:[1,0]
	v_pk_mul_f32 v[114:115], v[114:115], s[94:95] op_sel_hi:[1,0]
	v_add_u32_e32 v2, 0x30c0, v15
	ds_write2_b32 v2, v112, v113 offset1:1
	ds_write2_b32 v2, v114, v115 offset0:2 offset1:3
	s_waitcnt vmcnt(4)
	v_pk_mul_f32 v[116:117], v[116:117], s[94:95] op_sel_hi:[1,0]
	v_pk_mul_f32 v[118:119], v[118:119], s[94:95] op_sel_hi:[1,0]
	v_add_u32_e32 v2, 0x34d0, v15
	ds_write2_b32 v2, v116, v117 offset1:1
	ds_write2_b32 v2, v118, v119 offset0:2 offset1:3
	s_waitcnt vmcnt(3)
; #define GAS __attribute__((address_space(1)))
; #define LAS __attribute__((address_space(3)))
; #define LDS_WAIT() asm volatile("s_waitcnt lgkmcnt(0)" ::: "memory")
;     ...
;         LAS float* d = scr + kk * 65 + 4 * c4; d[0] = v[0]; d[1] = v[1]; d[2] = v[2]; d[3] = v[3]; }
;     LDS_WAIT(); asm volatile("" ::: "memory");
;     const int c = lane & 3;
; #pragma unroll
;     for (int j = 0; j < 4; ++j) { const int n = (lane >> 2) + 16 * j; const LAS float* s = scr + (16 * c) * 65 + n;
;         v4u o; o.x = pg8::pk4_fp8(s[0 * 65], s[1 * 65], s[2 * 65], s[3 * 65]); o.y = pg8::pk4_fp8(s[4 * 65], s[5 * 65], s[6 * 65], s[7 * 65]);
;         o.z = pg8::pk4_fp8(s[8 * 65], s[9 * 65], s[10 * 65], s[11 * 65]); o.w = pg8::pk4_fp8(s[12 * 65], s[13 * 65], s[14 * 65], s[15 * 65]);
;         *(GAS v4u*)(WT + ((size_t)((n0 + n) >> 4) * (K >> 5) + ((k0 + 16 * c) >> 5)) * 512 + ((n0 + n) & 15) * 32 + ((16 * c) & 31)) = o; }
	v_pk_mul_f32 v[120:121], v[120:121], s[94:95] op_sel_hi:[1,0]
	v_pk_mul_f32 v[122:123], v[122:123], s[94:95] op_sel_hi:[1,0]
	v_add_u32_e32 v2, 0x38e0, v15
	ds_write2_b32 v2, v120, v121 offset1:1
	ds_write2_b32 v2, v122, v123 offset0:2 offset1:3
	s_waitcnt vmcnt(2)
	v_pk_mul_f32 v[124:125], v[124:125], s[94:95] op_sel_hi:[1,0]
	v_pk_mul_f32 v[126:127], v[126:127], s[94:95] op_sel_hi:[1,0]
	v_add_u32_e32 v2, 0x3cf0, v15
	ds_write2_b32 v2, v124, v125 offset1:1
	ds_write2_b32 v2, v126, v127 offset0:2 offset1:3
	v_and_b32_e32 v2, 48, v5
	s_waitcnt lgkmcnt(0)
	v_mul_u32_u24_e32 v10, 0x104, v2
	v_and_b32_e32 v8, 16, v5
	v_and_b32_e32 v5, -4, v23
	v_add3_u32 v5, s82, v10, v5
	ds_read2_b32 v[12:13], v5 offset1:16
	v_ashrrev_i32_e32 v15, 2, v23
	v_lshlrev_b32_e32 v6, 5, v15
	v_readlane_b32 s18, v253, 58
	v_and_b32_e32 v6, 0x1e0, v6
	v_mov_b32_e32 v7, v3
	v_readlane_b32 s19, v253, 59
	ds_read2_b32 v[16:17], v5 offset0:65 offset1:81
	ds_read2_b32 v[18:19], v5 offset0:130 offset1:146
	ds_read2_b32 v[20:21], v5 offset0:195 offset1:211
	v_lshl_add_u64 v[6:7], s[18:19], 0, v[6:7]
	v_mov_b32_e32 v9, v3
	v_lshl_add_u64 v[6:7], v[6:7], 0, v[8:9]
	s_waitcnt lgkmcnt(3)
	v_max_f32_e32 v8, v12, v12
	v_med3_f32 v9, v8, s95, v199
	s_waitcnt lgkmcnt(2)
	v_max_f32_e32 v8, v16, v16
	v_med3_f32 v10, v8, s95, v199
	s_waitcnt lgkmcnt(1)
	v_max_f32_e32 v8, v18, v18
	v_add_u32_e32 v22, 0x400, v5
	v_med3_f32 v11, v8, s95, v199
	v_mov_b32_e32 v8, v3
	ds_read2_b32 v[24:25], v22 offset0:4 offset1:20
	v_cvt_pk_fp8_f32 v8, v9, v10
	s_waitcnt lgkmcnt(1)
	v_max_f32_e32 v12, v20, v20
	ds_read2_b32 v[26:27], v22 offset0:69 offset1:85
	ds_read2_b32 v[28:29], v22 offset0:134 offset1:150
	ds_read2_b32 v[30:31], v22 offset0:199 offset1:215
	v_med3_f32 v9, v12, s95, v199
	v_cvt_pk_fp8_f32 v8, v11, v9 op_sel:[0,0,1]
	s_waitcnt lgkmcnt(3)
	v_max_f32_e32 v9, v24, v24
	v_med3_f32 v10, v9, s95, v199
	s_waitcnt lgkmcnt(2)
	v_max_f32_e32 v9, v26, v26
	v_med3_f32 v11, v9, s95, v199
	s_waitcnt lgkmcnt(1)
	v_max_f32_e32 v9, v28, v28
	v_add_u32_e32 v52, 0x800, v5
	v_med3_f32 v12, v9, s95, v199
	v_mov_b32_e32 v9, v3
	ds_read2_b32 v[32:33], v52 offset0:8 offset1:24
	v_cvt_pk_fp8_f32 v9, v10, v11
	s_waitcnt lgkmcnt(1)
	v_max_f32_e32 v16, v30, v30
	ds_read2_b32 v[34:35], v52 offset0:73 offset1:89
	ds_read2_b32 v[36:37], v52 offset0:138 offset1:154
	ds_read2_b32 v[38:39], v52 offset0:203 offset1:219
	v_med3_f32 v10, v16, s95, v199
	v_cvt_pk_fp8_f32 v9, v12, v10 op_sel:[0,0,1]
	s_waitcnt lgkmcnt(3)
	v_max_f32_e32 v10, v32, v32
	v_med3_f32 v11, v10, s95, v199
	s_waitcnt lgkmcnt(2)
	v_max_f32_e32 v10, v34, v34
	v_med3_f32 v12, v10, s95, v199
	s_waitcnt lgkmcnt(1)
	v_max_f32_e32 v10, v36, v36
	v_add_u32_e32 v53, 0xc00, v5
	v_med3_f32 v16, v10, s95, v199
	v_mov_b32_e32 v10, v3
	ds_read2_b32 v[40:41], v53 offset0:12 offset1:28
	v_cvt_pk_fp8_f32 v10, v11, v12
	s_waitcnt lgkmcnt(1)
	v_max_f32_e32 v18, v38, v38
	ds_read2_b32 v[42:43], v53 offset0:77 offset1:93
	ds_read2_b32 v[44:45], v53 offset0:142 offset1:158
	ds_read2_b32 v[46:47], v53 offset0:207 offset1:223
	v_med3_f32 v11, v18, s95, v199
	v_cvt_pk_fp8_f32 v10, v16, v11 op_sel:[0,0,1]
	s_waitcnt lgkmcnt(3)
	v_max_f32_e32 v11, v40, v40
	v_med3_f32 v12, v11, s95, v199
	s_waitcnt lgkmcnt(2)
	v_max_f32_e32 v11, v42, v42
	v_med3_f32 v16, v11, s95, v199
	v_mov_b32_e32 v11, v3
	v_cvt_pk_fp8_f32 v11, v12, v16
	s_waitcnt lgkmcnt(1)
	v_max_f32_e32 v18, v44, v44
	s_waitcnt lgkmcnt(0)
	v_max_f32_e32 v16, v46, v46
	v_add_u32_e32 v15, s4, v15
	s_andn2_b32 s5, s5, 63
	v_med3_f32 v12, v18, s95, v199
	v_med3_f32 v16, v16, s95, v199
	v_ashrrev_i32_e32 v48, 4, v15
	v_or_b32_e32 v2, s5, v2
	v_cvt_pk_fp8_f32 v11, v12, v16 op_sel:[0,0,1]
	v_ashrrev_i32_e32 v49, 31, v48
	v_lshrrev_b32_e32 v2, 5, v2
	v_lshlrev_b64 v[48:49], 18, v[48:49]
	v_lshlrev_b64 v[50:51], 9, v[2:3]
	v_lshl_add_u64 v[48:49], v[6:7], 0, v[48:49]
	v_lshl_add_u64 v[48:49], v[48:49], 0, v[50:51]
	global_store_dwordx4 v[48:49], v[8:11], off
	v_max_f32_e32 v2, v13, v13
	v_med3_f32 v2, v2, s95, v199
	v_max_f32_e32 v8, v17, v17
	v_med3_f32 v9, v8, s95, v199
	v_mov_b32_e32 v8, v3
	v_cvt_pk_fp8_f32 v8, v2, v9
	v_max_f32_e32 v10, v19, v19
	v_max_f32_e32 v9, v21, v21
	v_med3_f32 v2, v10, s95, v199
	v_med3_f32 v9, v9, s95, v199
	v_cvt_pk_fp8_f32 v8, v2, v9 op_sel:[0,0,1]
	v_max_f32_e32 v2, v25, v25
	v_max_f32_e32 v9, v27, v27
	v_med3_f32 v2, v2, s95, v199
	v_med3_f32 v10, v9, s95, v199
	v_mov_b32_e32 v9, v3
	v_cvt_pk_fp8_f32 v9, v2, v10
	v_max_f32_e32 v11, v29, v29
	v_max_f32_e32 v10, v31, v31
	v_med3_f32 v2, v11, s95, v199
	v_med3_f32 v10, v10, s95, v199
	v_cvt_pk_fp8_f32 v9, v2, v10 op_sel:[0,0,1]
	v_max_f32_e32 v2, v33, v33
	v_max_f32_e32 v10, v35, v35
	v_med3_f32 v2, v2, s95, v199
	v_med3_f32 v11, v10, s95, v199
	v_mov_b32_e32 v10, v3
	v_cvt_pk_fp8_f32 v10, v2, v11
	v_max_f32_e32 v12, v37, v37
	v_max_f32_e32 v11, v39, v39
	v_med3_f32 v2, v12, s95, v199
	v_med3_f32 v11, v11, s95, v199
	v_cvt_pk_fp8_f32 v10, v2, v11 op_sel:[0,0,1]
	v_max_f32_e32 v2, v41, v41
	v_max_f32_e32 v11, v43, v43
	v_med3_f32 v2, v2, s95, v199
	v_med3_f32 v12, v11, s95, v199
	v_mov_b32_e32 v11, v3
	v_cvt_pk_fp8_f32 v11, v2, v12
	v_max_f32_e32 v13, v45, v45
	v_max_f32_e32 v12, v47, v47
	v_med3_f32 v2, v13, s95, v199
	v_med3_f32 v12, v12, s95, v199
	v_cvt_pk_fp8_f32 v11, v2, v12 op_sel:[0,0,1]
	v_add_u32_e32 v2, 16, v15
	v_ashrrev_i32_e32 v12, 4, v2
	v_ashrrev_i32_e32 v13, 31, v12
	v_lshlrev_b64 v[12:13], 18, v[12:13]
	v_lshl_add_u64 v[12:13], v[6:7], 0, v[12:13]
	v_lshl_add_u64 v[12:13], v[12:13], 0, v[50:51]
	ds_read2_b32 v[16:17], v5 offset0:32 offset1:48
	global_store_dwordx4 v[12:13], v[8:11], off
	ds_read2_b32 v[12:13], v5 offset0:97 offset1:113
	ds_read2_b32 v[18:19], v5 offset0:162 offset1:178
	ds_read2_b32 v[20:21], v5 offset0:227 offset1:243
	ds_read2_b32 v[24:25], v22 offset0:36 offset1:52
	ds_read2_b32 v[26:27], v22 offset0:101 offset1:117
	ds_read2_b32 v[28:29], v22 offset0:166 offset1:182
	ds_read2_b32 v[30:31], v22 offset0:231 offset1:247
	s_waitcnt lgkmcnt(7)
; #define GAS __attribute__((address_space(1)))
; #define LAS __attribute__((address_space(3)))
; #define LDS_WAIT() asm volatile("s_waitcnt lgkmcnt(0)" ::: "memory")
;     ...
;     const int c = lane & 3;
; #pragma unroll
;     for (int j = 0; j < 4; ++j) { const int n = (lane >> 2) + 16 * j; const LAS float* s = scr + (16 * c) * 65 + n;
;         v4u o; o.x = pg8::pk4_fp8(s[0 * 65], s[1 * 65], s[2 * 65], s[3 * 65]); o.y = pg8::pk4_fp8(s[4 * 65], s[5 * 65], s[6 * 65], s[7 * 65]);
;         o.z = pg8::pk4_fp8(s[8 * 65], s[9 * 65], s[10 * 65], s[11 * 65]); o.w = pg8::pk4_fp8(s[12 * 65], s[13 * 65], s[14 * 65], s[15 * 65]);
;         *(GAS v4u*)(WT + ((size_t)((n0 + n) >> 4) * (K >> 5) + ((k0 + 16 * c) >> 5)) * 512 + ((n0 + n) & 15) * 32 + ((16 * c) & 31)) = o; }
;     LDS_WAIT(); asm volatile("" ::: "memory");
	v_max_f32_e32 v2, v16, v16
	s_waitcnt lgkmcnt(6)
	v_max_f32_e32 v5, v12, v12
	s_waitcnt lgkmcnt(5)
	v_max_f32_e32 v8, v18, v18
	v_med3_f32 v2, v2, s95, v199
	v_med3_f32 v5, v5, s95, v199
	v_med3_f32 v9, v8, s95, v199
	v_mov_b32_e32 v8, v3
	v_cvt_pk_fp8_f32 v8, v2, v5
	s_waitcnt lgkmcnt(4)
	v_max_f32_e32 v2, v20, v20
	v_med3_f32 v2, v2, s95, v199
	s_waitcnt lgkmcnt(2)
	v_max_f32_e32 v5, v26, v26
	v_cvt_pk_fp8_f32 v8, v9, v2 op_sel:[0,0,1]
	v_max_f32_e32 v2, v24, v24
	s_waitcnt lgkmcnt(1)
	v_max_f32_e32 v9, v28, v28
	v_med3_f32 v2, v2, s95, v199
	v_med3_f32 v5, v5, s95, v199
	v_med3_f32 v10, v9, s95, v199
	v_mov_b32_e32 v9, v3
	ds_read2_b32 v[32:33], v52 offset0:40 offset1:56
	v_cvt_pk_fp8_f32 v9, v2, v5
	ds_read2_b32 v[34:35], v52 offset0:105 offset1:121
	ds_read2_b32 v[36:37], v52 offset0:170 offset1:186
	ds_read2_b32 v[38:39], v52 offset0:235 offset1:251
	s_waitcnt lgkmcnt(4)
	v_max_f32_e32 v2, v30, v30
	v_med3_f32 v2, v2, s95, v199
	v_cvt_pk_fp8_f32 v9, v10, v2 op_sel:[0,0,1]
	s_waitcnt lgkmcnt(3)
	v_max_f32_e32 v2, v32, v32
	s_waitcnt lgkmcnt(2)
	v_max_f32_e32 v5, v34, v34
	s_waitcnt lgkmcnt(1)
	v_max_f32_e32 v10, v36, v36
	v_med3_f32 v2, v2, s95, v199
	v_med3_f32 v5, v5, s95, v199
	v_med3_f32 v11, v10, s95, v199
	v_mov_b32_e32 v10, v3
	ds_read2_b32 v[40:41], v53 offset0:44 offset1:60
	v_cvt_pk_fp8_f32 v10, v2, v5
	ds_read2_b32 v[42:43], v53 offset0:109 offset1:125
	ds_read2_b32 v[44:45], v53 offset0:174 offset1:190
	ds_read2_b32 v[46:47], v53 offset0:239 offset1:255
	s_waitcnt lgkmcnt(4)
	v_max_f32_e32 v2, v38, v38
	v_med3_f32 v2, v2, s95, v199
	v_cvt_pk_fp8_f32 v10, v11, v2 op_sel:[0,0,1]
	s_waitcnt lgkmcnt(3)
	v_max_f32_e32 v2, v40, v40
	s_waitcnt lgkmcnt(2)
	v_max_f32_e32 v5, v42, v42
	v_med3_f32 v2, v2, s95, v199
	v_med3_f32 v5, v5, s95, v199
	v_mov_b32_e32 v11, v3
	v_cvt_pk_fp8_f32 v11, v2, v5
	s_waitcnt lgkmcnt(1)
	v_max_f32_e32 v12, v44, v44
	s_waitcnt lgkmcnt(0)
	v_max_f32_e32 v5, v46, v46
	v_med3_f32 v2, v12, s95, v199
	v_med3_f32 v5, v5, s95, v199
	v_cvt_pk_fp8_f32 v11, v2, v5 op_sel:[0,0,1]
	v_add_u32_e32 v2, 32, v15
	v_ashrrev_i32_e32 v48, 4, v2
	v_ashrrev_i32_e32 v49, 31, v48
	v_lshlrev_b64 v[48:49], 18, v[48:49]
	v_lshl_add_u64 v[48:49], v[6:7], 0, v[48:49]
	v_lshl_add_u64 v[48:49], v[48:49], 0, v[50:51]
	v_max_f32_e32 v2, v17, v17
	v_max_f32_e32 v5, v13, v13
	global_store_dwordx4 v[48:49], v[8:11], off
	v_med3_f32 v2, v2, s95, v199
	v_med3_f32 v5, v5, s95, v199
	v_mov_b32_e32 v8, v3
	v_cvt_pk_fp8_f32 v8, v2, v5
	v_max_f32_e32 v9, v19, v19
	v_max_f32_e32 v5, v21, v21
	v_med3_f32 v2, v9, s95, v199
	v_med3_f32 v5, v5, s95, v199
	v_cvt_pk_fp8_f32 v8, v2, v5 op_sel:[0,0,1]
	v_max_f32_e32 v2, v25, v25
	v_max_f32_e32 v5, v27, v27
	v_med3_f32 v2, v2, s95, v199
	v_med3_f32 v5, v5, s95, v199
	v_mov_b32_e32 v9, v3
	v_cvt_pk_fp8_f32 v9, v2, v5
	v_max_f32_e32 v10, v29, v29
	v_max_f32_e32 v5, v31, v31
	v_med3_f32 v2, v10, s95, v199
	v_med3_f32 v5, v5, s95, v199
	v_cvt_pk_fp8_f32 v9, v2, v5 op_sel:[0,0,1]
	v_max_f32_e32 v2, v33, v33
	v_max_f32_e32 v5, v35, v35
	v_med3_f32 v2, v2, s95, v199
	v_med3_f32 v5, v5, s95, v199
	v_mov_b32_e32 v10, v3
	v_cvt_pk_fp8_f32 v10, v2, v5
	v_max_f32_e32 v11, v37, v37
	v_max_f32_e32 v5, v39, v39
	v_med3_f32 v2, v11, s95, v199
	v_med3_f32 v5, v5, s95, v199
	v_cvt_pk_fp8_f32 v10, v2, v5 op_sel:[0,0,1]
	v_max_f32_e32 v2, v41, v41
	v_max_f32_e32 v5, v43, v43
	v_med3_f32 v2, v2, s95, v199
	v_med3_f32 v5, v5, s95, v199
	v_mov_b32_e32 v11, v3
	v_cvt_pk_fp8_f32 v11, v2, v5
	v_max_f32_e32 v12, v45, v45
	v_max_f32_e32 v5, v47, v47
	v_med3_f32 v2, v12, s95, v199
	v_med3_f32 v5, v5, s95, v199
	v_cvt_pk_fp8_f32 v11, v2, v5 op_sel:[0,0,1]
	v_add_u32_e32 v2, 48, v15
	v_ashrrev_i32_e32 v12, 4, v2
	v_ashrrev_i32_e32 v13, 31, v12
	v_lshlrev_b64 v[12:13], 18, v[12:13]
	v_lshl_add_u64 v[6:7], v[6:7], 0, v[12:13]
	v_lshl_add_u64 v[6:7], v[6:7], 0, v[50:51]
	global_store_dwordx4 v[6:7], v[8:11], off
	s_waitcnt lgkmcnt(0)
	s_mov_b64 s[4:5], 0

; #define GAS __attribute__((address_space(1)))
; #define LAS __attribute__((address_space(3)))
;     const int nblk = N / 64, kb = item / nblk, nb = item - kb * nblk, k0 = 64 * kb, n0 = 64 * nb; if (ldw == 0) ldw = N;
;     const int c4 = lane & 15, kq = lane >> 4;
; #pragma unroll 4
;     for (int i = 0; i < 16; ++i) { const int kk = 4 * i + kq;
;         f32x4 v = __builtin_nontemporal_load((const GAS f32x4*)(W + (size_t)(k0 + kk) * ldw + n0 + 4 * c4));
;         v = v * (gk ? gk[k0 + kk] * scale : scale);
;         LAS float* d = scr + kk * 65 + 4 * c4; d[0] = v[0]; d[1] = v[1]; d[2] = v[2]; d[3] = v[3]; }
.Lconv_gdone_up:
	global_load_dwordx4 v[64:67], v[16:17], off nt
	v_lshl_add_u64 v[16:17], v[16:17], 0, s[100:101]
	global_load_dwordx4 v[68:71], v[16:17], off nt
	v_lshl_add_u64 v[16:17], v[16:17], 0, s[100:101]
	global_load_dwordx4 v[72:75], v[16:17], off nt
	v_lshl_add_u64 v[16:17], v[16:17], 0, s[100:101]
	global_load_dwordx4 v[76:79], v[16:17], off nt
	v_lshl_add_u64 v[16:17], v[16:17], 0, s[100:101]
	global_load_dwordx4 v[80:83], v[16:17], off nt
	v_lshl_add_u64 v[16:17], v[16:17], 0, s[100:101]
	global_load_dwordx4 v[84:87], v[16:17], off nt
	v_lshl_add_u64 v[16:17], v[16:17], 0, s[100:101]
	global_load_dwordx4 v[88:91], v[16:17], off nt
	v_lshl_add_u64 v[16:17], v[16:17], 0, s[100:101]
	global_load_dwordx4 v[92:95], v[16:17], off nt
	v_lshl_add_u64 v[16:17], v[16:17], 0, s[100:101]
	global_load_dwordx4 v[96:99], v[16:17], off nt
	v_lshl_add_u64 v[16:17], v[16:17], 0, s[100:101]
	global_load_dwordx4 v[100:103], v[16:17], off nt
	v_lshl_add_u64 v[16:17], v[16:17], 0, s[100:101]
	global_load_dwordx4 v[104:107], v[16:17], off nt
	v_lshl_add_u64 v[16:17], v[16:17], 0, s[100:101]
	global_load_dwordx4 v[108:111], v[16:17], off nt
	v_lshl_add_u64 v[16:17], v[16:17], 0, s[100:101]
	global_load_dwordx4 v[112:115], v[16:17], off nt
	v_lshl_add_u64 v[16:17], v[16:17], 0, s[100:101]
	global_load_dwordx4 v[116:119], v[16:17], off nt
	v_lshl_add_u64 v[16:17], v[16:17], 0, s[100:101]
	global_load_dwordx4 v[120:123], v[16:17], off nt
	v_lshl_add_u64 v[16:17], v[16:17], 0, s[100:101]
	global_load_dwordx4 v[124:127], v[16:17], off nt
	s_cmp_lt_u32 s29, 0x5000
	s_cselect_b64 s[98:99], -1, 0
	v_lshrrev_b32_e32 v195, 4, v23
	v_sub_u32_e32 v196, v23, v195
	v_lshlrev_b32_e32 v196, 16, v196
	v_and_b32_e32 v195, 15, v23
	v_lshlrev_b32_e32 v195, 4, v195
	v_sub_u32_e32 v196, v196, v195
	v_add_u32_e32 v196, 0x1c40000, v196
	v_mov_b32_e32 v195, 0xffffff80
	v_cndmask_b32_e64 v196, v195, v196, s[98:99]
	v_ashrrev_i32_e32 v197, 31, v196
	v_lshl_add_u64 v[196:197], v[16:17], 0, v[196:197]
	global_load_dword v195, v[196:197], off
	global_load_dword v195, v[196:197], off offset:128
	s_waitcnt vmcnt(17)
	v_mul_f32_e32 v164, 0x42800000, v164
	v_pk_mul_f32 v[64:65], v[64:65], v[164:165] op_sel_hi:[1,0]
	v_pk_mul_f32 v[66:67], v[66:67], v[164:165] op_sel_hi:[1,0]
	ds_write2_b32 v25, v64, v65 offset1:1
	ds_write2_b32 v25, v66, v67 offset0:2 offset1:3
	s_waitcnt vmcnt(16)
	v_mul_f32_e32 v166, 0x42800000, v166
	v_pk_mul_f32 v[68:69], v[68:69], v[166:167] op_sel_hi:[1,0]
	v_pk_mul_f32 v[70:71], v[70:71], v[166:167] op_sel_hi:[1,0]
	v_add_u32_e32 v2, 0x410, v25
	ds_write2_b32 v2, v68, v69 offset1:1
	ds_write2_b32 v2, v70, v71 offset0:2 offset1:3
	s_waitcnt vmcnt(15)
	v_mul_f32_e32 v168, 0x42800000, v168
	v_pk_mul_f32 v[72:73], v[72:73], v[168:169] op_sel_hi:[1,0]
	v_pk_mul_f32 v[74:75], v[74:75], v[168:169] op_sel_hi:[1,0]
	v_add_u32_e32 v2, 0x820, v25
	ds_write2_b32 v2, v72, v73 offset1:1
	ds_write2_b32 v2, v74, v75 offset0:2 offset1:3
	s_waitcnt vmcnt(14)
	v_mul_f32_e32 v170, 0x42800000, v170
	v_pk_mul_f32 v[76:77], v[76:77], v[170:171] op_sel_hi:[1,0]
	v_pk_mul_f32 v[78:79], v[78:79], v[170:171] op_sel_hi:[1,0]
	v_add_u32_e32 v2, 0xc30, v25
	ds_write2_b32 v2, v76, v77 offset1:1
	ds_write2_b32 v2, v78, v79 offset0:2 offset1:3
	s_waitcnt vmcnt(13)
	v_mul_f32_e32 v172, 0x42800000, v172
	v_pk_mul_f32 v[80:81], v[80:81], v[172:173] op_sel_hi:[1,0]
	v_pk_mul_f32 v[82:83], v[82:83], v[172:173] op_sel_hi:[1,0]
	v_add_u32_e32 v2, 0x1040, v25
	ds_write2_b32 v2, v80, v81 offset1:1
	ds_write2_b32 v2, v82, v83 offset0:2 offset1:3
	s_waitcnt vmcnt(12)
	v_mul_f32_e32 v174, 0x42800000, v174
	v_pk_mul_f32 v[84:85], v[84:85], v[174:175] op_sel_hi:[1,0]
	v_pk_mul_f32 v[86:87], v[86:87], v[174:175] op_sel_hi:[1,0]
	v_add_u32_e32 v2, 0x1450, v25
	ds_write2_b32 v2, v84, v85 offset1:1
	ds_write2_b32 v2, v86, v87 offset0:2 offset1:3
	s_waitcnt vmcnt(11)
	v_mul_f32_e32 v176, 0x42800000, v176
	v_pk_mul_f32 v[88:89], v[88:89], v[176:177] op_sel_hi:[1,0]
	v_pk_mul_f32 v[90:91], v[90:91], v[176:177] op_sel_hi:[1,0]
	v_add_u32_e32 v2, 0x1860, v25
	ds_write2_b32 v2, v88, v89 offset1:1
	ds_write2_b32 v2, v90, v91 offset0:2 offset1:3
	s_waitcnt vmcnt(10)
	v_mul_f32_e32 v178, 0x42800000, v178
	v_pk_mul_f32 v[92:93], v[92:93], v[178:179] op_sel_hi:[1,0]
	v_pk_mul_f32 v[94:95], v[94:95], v[178:179] op_sel_hi:[1,0]
	v_add_u32_e32 v2, 0x1c70, v25
	ds_write2_b32 v2, v92, v93 offset1:1
	ds_write2_b32 v2, v94, v95 offset0:2 offset1:3
	s_waitcnt vmcnt(9)
	v_mul_f32_e32 v180, 0x42800000, v180
	v_pk_mul_f32 v[96:97], v[96:97], v[180:181] op_sel_hi:[1,0]
	v_pk_mul_f32 v[98:99], v[98:99], v[180:181] op_sel_hi:[1,0]
	v_add_u32_e32 v2, 0x2080, v25
	ds_write2_b32 v2, v96, v97 offset1:1
	ds_write2_b32 v2, v98, v99 offset0:2 offset1:3
	s_waitcnt vmcnt(8)
	v_mul_f32_e32 v182, 0x42800000, v182
	v_pk_mul_f32 v[100:101], v[100:101], v[182:183] op_sel_hi:[1,0]
	v_pk_mul_f32 v[102:103], v[102:103], v[182:183] op_sel_hi:[1,0]
	v_add_u32_e32 v2, 0x2490, v25
	ds_write2_b32 v2, v100, v101 offset1:1
	ds_write2_b32 v2, v102, v103 offset0:2 offset1:3
	s_waitcnt vmcnt(7)
	v_mul_f32_e32 v184, 0x42800000, v184
	v_pk_mul_f32 v[104:105], v[104:105], v[184:185] op_sel_hi:[1,0]
	v_pk_mul_f32 v[106:107], v[106:107], v[184:185] op_sel_hi:[1,0]
	v_add_u32_e32 v2, 0x28a0, v25
	ds_write2_b32 v2, v104, v105 offset1:1
	ds_write2_b32 v2, v106, v107 offset0:2 offset1:3
	s_waitcnt vmcnt(6)
	v_mul_f32_e32 v186, 0x42800000, v186
	v_pk_mul_f32 v[108:109], v[108:109], v[186:187] op_sel_hi:[1,0]
	v_pk_mul_f32 v[110:111], v[110:111], v[186:187] op_sel_hi:[1,0]
	v_add_u32_e32 v2, 0x2cb0, v25
	ds_write2_b32 v2, v108, v109 offset1:1
	ds_write2_b32 v2, v110, v111 offset0:2 offset1:3
	s_waitcnt vmcnt(5)
	v_mul_f32_e32 v188, 0x42800000, v188
	v_pk_mul_f32 v[112:113], v[112:113], v[188:189] op_sel_hi:[1,0]
	v_pk_mul_f32 v[114:115], v[114:115], v[188:189] op_sel_hi:[1,0]
	v_add_u32_e32 v2, 0x30c0, v25
	ds_write2_b32 v2, v112, v113 offset1:1
	ds_write2_b32 v2, v114, v115 offset0:2 offset1:3
	s_waitcnt vmcnt(4)
	v_mul_f32_e32 v190, 0x42800000, v190
	v_pk_mul_f32 v[116:117], v[116:117], v[190:191] op_sel_hi:[1,0]
	v_pk_mul_f32 v[118:119], v[118:119], v[190:191] op_sel_hi:[1,0]
	v_add_u32_e32 v2, 0x34d0, v25
	ds_write2_b32 v2, v116, v117 offset1:1
	ds_write2_b32 v2, v118, v119 offset0:2 offset1:3
	s_waitcnt vmcnt(3)
	v_mul_f32_e32 v192, 0x42800000, v192
	v_pk_mul_f32 v[120:121], v[120:121], v[192:193] op_sel_hi:[1,0]
	v_pk_mul_f32 v[122:123], v[122:123], v[192:193] op_sel_hi:[1,0]
	v_add_u32_e32 v2, 0x38e0, v25
	ds_write2_b32 v2, v120, v121 offset1:1
	ds_write2_b32 v2, v122, v123 offset0:2 offset1:3
	s_waitcnt vmcnt(2)
	v_mul_f32_e32 v194, 0x42800000, v194
	v_pk_mul_f32 v[124:125], v[124:125], v[194:195] op_sel_hi:[1,0]
	v_pk_mul_f32 v[126:127], v[126:127], v[194:195] op_sel_hi:[1,0]
	v_add_u32_e32 v2, 0x3cf0, v25
	ds_write2_b32 v2, v124, v125 offset1:1
	ds_write2_b32 v2, v126, v127 offset0:2 offset1:3
